# Fourier stage B unit loop: the wait before staging the prefetched tile now counts only the prefetch loads (vmcnt 8), not the previous unit's eight output stores; plus previous changes
# speedup vs baseline: 1.0018x; 1.0018x over previous
; #define LAS __attribute__((address_space(3)))
;     __device__ __forceinline__ bf16_t* dft() const { return (bf16_t*)(ws + WS_DFT); }
;     __device__ __forceinline__ bf16_t* dn() const { return (bf16_t*)(ws + WS_DN); }
; #define FB_LOAD(u) do { const int _b = (u) >> 9, _k1 = ((u) >> 2) & 127, _cb = (u) & 3; \
;         _Pragma("unroll") for (int _q = 0; _q < 4; ++_q) pf[_q] = *(const bf16x8*)(F.zm() + (size_t)((_b * 128 + _k1) * 64 + (_q & 1) * 32 + sr) * DM + (_q >> 1) * 512 + _cb * 128 + sc); } while (0)
; __device__ __forceinline__ void phase_fft_b(const Frame& F) {
;     const int tid = F.tid, wid = F.wid, lane = F.lane, r32 = lane & 31, hi = lane >> 5;
;     LAS char* Vt = (LAS char*)F.lds;
;     const int sr = tid >> 4, sc = (tid & 15) * 8;
;     const int rb = wid & 1, cq = wid >> 1, k2 = 32 * rb + r32;
;     const bf16_t* dc = F.dft() + 32768; const bf16_t* ds = dc + 4096; const bf16_t* dn = dc + 8192;
;     bf16x8 bc[4], bs[4], bn[4];
; #pragma unroll
;     for (int ks = 0; ks < 4; ++ks) { const int o = k2 * 64 + ks * 16 + hi * 8; bc[ks] = *(const bf16x8*)(dc + o); bs[ks] = *(const bf16x8*)(ds + o); bn[ks] = *(const bf16x8*)(dn + o); }
;     const int NU = NB * 128 * 4;
;     bf16x8 pf[4];
;     ...
;     int u = F.wg, par = 0;
;     if (u < NU) FB_LOAD(u);
.LBB0_508:
	s_andn2_b64 vcc, exec, s[8:9]
	s_cbranch_vccnz .LBB0_585
	v_readlane_b32 s8, v252, 42
	s_waitcnt vmcnt(0)
	v_mov_b32_e32 v2, v0
	v_readlane_b32 s9, v252, 43
	s_andn2_b64 vcc, exec, s[8:9]
	v_readfirstlane_b32 s0, v2
	v_mov_b32_e32 v136, 0xffff8000
	v_mov_b32_e32 v137, 0xffffa000
	v_mov_b32_e32 v138, 0xffffc000
	v_mov_b32_e32 v139, 0xa000
	v_mov_b32_e32 v140, 0xc000
	v_mov_b32_e32 v141, 0x10000
	v_mov_b32_e32 v142, 0x12000
	v_mov_b32_e32 v143, 0x14000
	v_mov_b32_e32 v144, 0x16000
	v_mov_b32_e32 v145, 0x18000
	v_mov_b32_e32 v148, 0x1a000
	v_mov_b32_e32 v149, 0x1c000
	s_cbranch_vccnz .LBB0_516
	s_lshr_b32 s1, s0, 1
	s_add_u32 s8, s56, 0xd0000
	v_and_b32_e32 v1, 31, v2
	s_addc_u32 s9, s57, 0
	v_and_or_b32 v1, s1, 32, v1
	s_add_u32 s18, s56, 0xd2000
	v_bfe_u32 v3, v2, 5, 1
	s_addc_u32 s19, s57, 0
	v_lshlrev_b32_e32 v1, 7, v1
	s_add_u32 s22, s56, 0xd4000
	v_lshl_or_b32 v4, v3, 4, v1
	v_ashrrev_i32_e32 v100, 4, v2
	v_readlane_b32 s1, v253, 1
	s_addc_u32 s23, s57, 0
	v_or_b32_e32 v5, 32, v4
	v_add_u32_e32 v6, s1, v100
	global_load_dwordx4 v[34:37], v4, s[8:9]
	global_load_dwordx4 v[38:41], v4, s[18:19]
	global_load_dwordx4 v[42:45], v4, s[22:23]
	global_load_dwordx4 v[46:49], v5, s[8:9]
	global_load_dwordx4 v[50:53], v5, s[18:19]
	global_load_dwordx4 v[54:57], v5, s[22:23]
	v_or_b32_e32 v5, 64, v4
	s_ashr_i32 s0, s0, 7
	v_ashrrev_i32_e32 v7, 31, v6
	global_load_dwordx4 v[58:61], v5, s[8:9]
	global_load_dwordx4 v[62:65], v5, s[18:19]
	v_or_b32_e32 v4, 0x60, v4
	global_load_dwordx4 v[66:69], v5, s[22:23]
	global_load_dwordx4 v[70:73], v4, s[8:9]
	global_load_dwordx4 v[74:77], v4, s[18:19]
	global_load_dwordx4 v[78:81], v4, s[22:23]
	s_add_u32 s8, s56, 0x3d316100
	v_lshlrev_b64 v[8:9], 11, v[6:7]
	v_add_u32_e32 v6, 32, v6
	v_lshlrev_b32_e32 v5, 3, v2
	s_addc_u32 s9, s57, 0
	v_readlane_b32 s1, v252, 57
	v_ashrrev_i32_e32 v7, 31, v6
	v_and_b32_e32 v4, 0x78, v5
	v_lshl_add_u64 v[8:9], s[8:9], 0, v[8:9]
	s_lshl_b32 s76, s1, 1
	v_lshlrev_b64 v[6:7], 11, v[6:7]
	v_lshl_add_u64 v[8:9], v[8:9], 0, s[76:77]
	v_lshlrev_b32_e32 v146, 1, v4
	v_lshl_add_u64 v[6:7], s[8:9], 0, v[6:7]
	v_lshl_add_u64 v[8:9], v[8:9], 0, v[146:147]
	v_lshl_add_u64 v[6:7], v[6:7], 0, s[76:77]
	v_lshl_add_u64 v[6:7], v[6:7], 0, v[146:147]
	global_load_dwordx4 v[82:85], v[8:9], off
	global_load_dwordx4 v[86:89], v[8:9], off offset:1024
	global_load_dwordx4 v[90:93], v[6:7], off
	global_load_dwordx4 v[94:97], v[6:7], off offset:1024
	v_lshrrev_b32_e32 v7, 1, v100
	v_and_b32_e32 v8, 3, v100
	v_and_b32_e32 v6, 63, v2
	v_and_or_b32 v7, v7, 4, v8
	v_lshlrev_b32_e32 v101, 6, v7
	v_lshlrev_b32_e32 v7, 4, v2
	v_lshlrev_b32_e32 v6, 3, v6
	v_and_b32_e32 v102, 48, v7
	v_and_b32_e32 v8, 24, v6
	v_and_b32_e32 v7, 0xc0, v7
	v_lshlrev_b32_e32 v2, 1, v2
	s_lshl_b32 s1, s0, 9
	v_and_b32_e32 v2, 32, v2
	v_and_b32_e32 v6, 0x100, v6
	v_or3_b32 v7, v7, s1, v8
	v_or3_b32 v103, v7, v2, v6
	v_lshlrev_b32_e32 v2, 2, v3
	v_and_b32_e32 v3, 0xfffff0, v100
	v_lshlrev_b32_e32 v6, 1, v100
	v_and_or_b32 v3, v6, 8, v3
	v_bfe_u32 v5, v5, 5, 2
	v_lshrrev_b32_e32 v3, 1, v3
	v_or_b32_e32 v3, v3, v5
	v_lshlrev_b32_e32 v104, 9, v3
	v_add_u32_e32 v3, 32, v100
	v_and_b32_e32 v6, 0xfffff0, v3
	v_lshlrev_b32_e32 v3, 1, v3
	s_lshl_b32 s18, s0, 5
	v_and_or_b32 v3, v3, 8, v6
	s_ashr_i32 s19, s18, 31
	v_lshrrev_b32_e32 v3, 1, v3
	v_or_b32_e32 v3, v3, v5
	s_add_u32 s22, s56, 0x1c316100
	v_readlane_b32 s24, v254, 62
	v_lshlrev_b32_e32 v105, 9, v3
	s_addc_u32 s23, s57, 0
	s_mov_b32 s0, 0
	v_lshlrev_b32_e32 v98, 1, v4
	v_lshlrev_b32_e32 v146, 1, v2
	v_readlane_b32 s1, v254, 6
	v_readlane_b32 s30, v253, 15
	s_mov_b32 s31, s24
	v_readlane_b32 s25, v254, 63
	s_waitcnt vmcnt(0)
	s_branch .LBB0_512

; #define LAS __attribute__((address_space(3)))
; __device__ __forceinline__ int v_st(int k, int c) { const int kk = (k & ~0xC) | ((k & 4) << 1) | ((k & 8) >> 1); return ((kk >> 3) * 4 + (c >> 5)) * 512 + ((kk & 7) * 32 + (c & 31)) * 2; }
; #define FB_LOAD(u) do { const int _b = (u) >> 9, _k1 = ((u) >> 2) & 127, _cb = (u) & 3; \
;         _Pragma("unroll") for (int _q = 0; _q < 4; ++_q) pf[_q] = *(const bf16x8*)(F.zm() + (size_t)((_b * 128 + _k1) * 64 + (_q & 1) * 32 + sr) * DM + (_q >> 1) * 512 + _cb * 128 + sc); } while (0)
; __device__ __forceinline__ void phase_fft_b(const Frame& F) {
;     ...
;     for (; u < NU; u += F.nwg, par ^= 1) {
;         const int b = u >> 9, k1 = (u >> 2) & 127, cb = u & 3;
;         LAS char* img = Vt + par * 32768;
; #pragma unroll
;         for (int q = 0; q < 4; ++q) *(LAS bf16x8*)(img + (q >> 1) * 16384 + ff::v_st((q & 1) * 32 + sr, sc)) = pf[q];
;         __syncthreads();
;         if (u + F.nwg < NU) FB_LOAD(u + F.nwg);
.LBB0_512:
	s_lshl_b32 s2, s0, 15
	s_add_i32 s40, s2, 0
	s_add_i32 s2, s31, s96
	v_add_u32_e32 v2, s40, v104
	v_add_u32_e32 v3, s40, v105
	s_cmpk_gt_i32 s2, 0xfff
	v_add3_u32 v2, v2, v101, v102
	v_add3_u32 v3, v3, v101, v102
	s_cselect_b64 s[24:25], -1, 0
	s_cmpk_lt_i32 s2, 0x1000
	s_mov_b64 s[28:29], -1
	s_waitcnt vmcnt(8)
	ds_write_b128 v2, v[82:85]
	ds_write_b128 v3, v[90:93]
	ds_write_b128 v2, v[86:89] offset:16384
	ds_write_b128 v3, v[94:97] offset:16384
	s_waitcnt lgkmcnt(0)
	s_barrier
	s_cbranch_scc1 .LBB0_514
	v_readlane_b32 s7, v254, 4
	s_add_i32 s7, s30, s7
	s_mov_b64 s[28:29], 0
